# RG-LRU conv stage: f32 conv writes use one base address register plus DS immediates (7 fewer VALU per chunk per wave)
# speedup vs baseline: 1.0040x; 1.0024x over previous
; #define LAS __attribute__((address_space(3)))
; __device__ __forceinline__ unsigned cvtpk(float lo, float hi) { const f32x2 v = {lo, hi}; return __builtin_bit_cast(unsigned, __builtin_convertvector(v, bf16x2_t)); }
; __device__ __forceinline__ void unit(LAS unsigned char* lds, const bf16* __restrict__ xr, const bf16* __restrict__ yg, const float* __restrict__ conv_w, const float* __restrict__ conv_b, const bf16* __restrict__ wga_t, const bf16* __restrict__ wgx_t, ...
;     ...
;         { f32x2 xe[11];
; #pragma unroll
;           for (int k = 0; k < 11; ++k) xe[k] = (f32x2){__uint_as_float(xq[k] << 16), __uint_as_float(xq[k] & 0xffff0000u)};
; #pragma unroll
;           for (int i = 0; i < 8; ++i) { f32x2 xc2 = (f32x2){cb0, cb1};
; #pragma unroll
;             for (int jj = 0; jj < 4; ++jj) xc2 += (f32x2){cw0[jj], cw1[jj]} * xe[i + jj];
;             *(LAS unsigned*)(lds + XA_OFF + (8 * wave + i) * XA_P + 4 * lane) = cvtpk(xc2.x, xc2.y);
;             if ((lane >> 5) == hf) *(LAS f32x2*)(XF + (8 * wave + i) * 64 + 2 * (lane & 31)) = xc2; } }
.LBB5_937:
	v_lshlrev_b32_e32 v84, 16, v137
	v_and_b32_e32 v85, 0xffff0000, v137
	v_lshlrev_b32_e32 v88, 16, v98
	v_and_b32_e32 v89, 0xffff0000, v98
	v_pk_fma_f32 v[84:85], v[112:113], v[84:85], v[114:115]
	v_lshlrev_b32_e32 v86, 16, v138
	v_and_b32_e32 v87, 0xffff0000, v138
	v_pk_fma_f32 v[84:85], v[108:109], v[88:89], v[84:85]
	v_lshlrev_b32_e32 v82, 16, v147
	v_and_b32_e32 v83, 0xffff0000, v147
	v_pk_fma_f32 v[84:85], v[110:111], v[86:87], v[84:85]
	s_nop 0
	v_pk_fma_f32 v[84:85], v[116:117], v[82:83], v[84:85]
	s_nop 0
	v_cvt_pk_bf16_f32 v90, v84, v85
	ds_write_b32 v156, v90
	s_and_saveexec_b64 s[68:69], s[6:7]
	v_add_u32_e32 v244, s80, v128
	ds_write_b64 v244, v[84:85] offset:17408
	s_or_b64 exec, exec, s[68:69]
	v_pk_fma_f32 v[88:89], v[112:113], v[88:89], v[114:115]
	v_lshlrev_b32_e32 v84, 16, v150
	v_pk_fma_f32 v[88:89], v[108:109], v[86:87], v[88:89]
	v_and_b32_e32 v85, 0xffff0000, v150
	v_pk_fma_f32 v[88:89], v[110:111], v[82:83], v[88:89]
	v_add_u32_e32 v90, s81, v126
	v_pk_fma_f32 v[88:89], v[116:117], v[84:85], v[88:89]
	s_nop 0
	v_cvt_pk_bf16_f32 v91, v88, v89
	ds_write_b32 v90, v91
	s_and_saveexec_b64 s[68:69], s[6:7]
	ds_write_b64 v244, v[88:89] offset:17664
	s_or_b64 exec, exec, s[68:69]
	v_pk_fma_f32 v[86:87], v[112:113], v[86:87], v[114:115]
	v_lshlrev_b32_e32 v88, 16, v146
	v_pk_fma_f32 v[86:87], v[108:109], v[82:83], v[86:87]
	v_and_b32_e32 v89, 0xffff0000, v146
	v_pk_fma_f32 v[86:87], v[110:111], v[84:85], v[86:87]
	s_nop 0
	v_pk_fma_f32 v[86:87], v[116:117], v[88:89], v[86:87]
	s_nop 0
	v_cvt_pk_bf16_f32 v91, v86, v87
	ds_write_b32 v90, v91 offset:272
	s_and_saveexec_b64 s[68:69], s[6:7]
	ds_write_b64 v244, v[86:87] offset:17920
	s_or_b64 exec, exec, s[68:69]
	v_pk_fma_f32 v[82:83], v[112:113], v[82:83], v[114:115]
	v_lshlrev_b32_e32 v86, 16, v151
	v_pk_fma_f32 v[82:83], v[108:109], v[84:85], v[82:83]
	v_and_b32_e32 v87, 0xffff0000, v151
	v_pk_fma_f32 v[82:83], v[110:111], v[88:89], v[82:83]
	s_nop 0
	v_pk_fma_f32 v[82:83], v[116:117], v[86:87], v[82:83]
	s_nop 0
	v_cvt_pk_bf16_f32 v91, v82, v83
	ds_write_b32 v90, v91 offset:544
	s_and_saveexec_b64 s[68:69], s[6:7]
	ds_write_b64 v244, v[82:83] offset:18176
	s_or_b64 exec, exec, s[68:69]
	v_pk_fma_f32 v[84:85], v[112:113], v[84:85], v[114:115]
	v_lshlrev_b32_e32 v82, 16, v157
	v_pk_fma_f32 v[84:85], v[108:109], v[88:89], v[84:85]
	v_and_b32_e32 v83, 0xffff0000, v157
	v_pk_fma_f32 v[84:85], v[110:111], v[86:87], v[84:85]
	s_nop 0
	v_pk_fma_f32 v[84:85], v[116:117], v[82:83], v[84:85]
	s_nop 0
	v_cvt_pk_bf16_f32 v91, v84, v85
	ds_write_b32 v90, v91 offset:816
	s_and_saveexec_b64 s[68:69], s[6:7]
	ds_write_b64 v244, v[84:85] offset:18432
	s_or_b64 exec, exec, s[68:69]
	v_pk_fma_f32 v[88:89], v[112:113], v[88:89], v[114:115]
	v_lshlrev_b32_e32 v84, 16, v158
	v_pk_fma_f32 v[88:89], v[108:109], v[86:87], v[88:89]
	v_and_b32_e32 v85, 0xffff0000, v158
	v_pk_fma_f32 v[88:89], v[110:111], v[82:83], v[88:89]
	s_nop 0
	v_pk_fma_f32 v[88:89], v[116:117], v[84:85], v[88:89]
	s_nop 0
	v_cvt_pk_bf16_f32 v91, v88, v89
	ds_write_b32 v90, v91 offset:1088
	s_and_saveexec_b64 s[68:69], s[6:7]
	ds_write_b64 v244, v[88:89] offset:18688
	s_or_b64 exec, exec, s[68:69]
	v_pk_fma_f32 v[86:87], v[112:113], v[86:87], v[114:115]
	v_lshlrev_b32_e32 v88, 16, v159
	v_pk_fma_f32 v[86:87], v[108:109], v[82:83], v[86:87]
	v_and_b32_e32 v89, 0xffff0000, v159
	v_pk_fma_f32 v[86:87], v[110:111], v[84:85], v[86:87]
	s_nop 0
	v_pk_fma_f32 v[86:87], v[116:117], v[88:89], v[86:87]
	s_nop 0
	v_cvt_pk_bf16_f32 v91, v86, v87
	ds_write_b32 v90, v91 offset:1360
	s_and_saveexec_b64 s[68:69], s[6:7]
	ds_write_b64 v244, v[86:87] offset:18944
	s_or_b64 exec, exec, s[68:69]
	v_pk_fma_f32 v[82:83], v[112:113], v[82:83], v[114:115]
	v_lshlrev_b32_e32 v86, 16, v160
	v_pk_fma_f32 v[82:83], v[108:109], v[84:85], v[82:83]
	v_and_b32_e32 v87, 0xffff0000, v160
	v_pk_fma_f32 v[82:83], v[110:111], v[88:89], v[82:83]
	s_nop 0
	v_pk_fma_f32 v[82:83], v[116:117], v[86:87], v[82:83]
	s_nop 0
	v_cvt_pk_bf16_f32 v84, v82, v83
	ds_write_b32 v90, v84 offset:1632
	s_and_saveexec_b64 s[68:69], s[6:7]
	ds_write_b64 v244, v[82:83] offset:19200
	s_or_b64 exec, exec, s[68:69]
	s_add_i32 s90, s90, 64
	s_cmpk_gt_u32 s90, 0x7bf
	s_cselect_b64 s[68:69], -1, 0
	s_and_b64 vcc, exec, s[68:69]
	s_cbranch_vccnz .LBB5_955
	v_lshl_add_u64 v[82:83], s[22:23], 0, v[118:119]
	v_add_co_u32_e32 v84, vcc, 0x4801e000, v82
	s_nop 1
	v_addc_co_u32_e32 v85, vcc, 0, v83, vcc
	global_load_dword v137, v[84:85], off offset:2048
	v_add_co_u32_e32 v84, vcc, 0x4801f000, v82
	s_nop 1
	v_addc_co_u32_e32 v85, vcc, 0, v83, vcc
	global_load_dword v98, v[84:85], off
	global_load_dword v138, v[84:85], off offset:2048
	v_add_co_u32_e32 v84, vcc, 0x48020000, v82
	s_nop 1
	v_addc_co_u32_e32 v85, vcc, 0, v83, vcc
	global_load_dword v147, v[84:85], off
	global_load_dword v150, v[84:85], off offset:2048
	v_add_co_u32_e32 v84, vcc, 0x48021000, v82
	s_nop 1
	v_addc_co_u32_e32 v85, vcc, 0, v83, vcc
	global_load_dword v146, v[84:85], off
	global_load_dword v151, v[84:85], off offset:2048
	v_add_co_u32_e32 v84, vcc, 0x48022000, v82
	s_nop 1
	v_addc_co_u32_e32 v85, vcc, 0, v83, vcc
	v_add_co_u32_e32 v82, vcc, 0x48023000, v82
	global_load_dword v157, v[84:85], off
	global_load_dword v158, v[84:85], off offset:2048
	v_addc_co_u32_e32 v83, vcc, 0, v83, vcc
	global_load_dword v159, v[82:83], off
	global_load_dword v160, v[82:83], off offset:2048
	v_lshl_add_u64 v[82:83], s[22:23], 0, v[120:121]
	v_add_co_u32_e32 v84, vcc, 0x4c020000, v82
	s_nop 1
	v_addc_co_u32_e32 v85, vcc, 0, v83, vcc
	global_load_ushort v167, v[84:85], off
	global_load_ushort v168, v[84:85], off offset:2048
	v_add_co_u32_e32 v84, vcc, 0x4c021000, v82
	s_nop 1
	v_addc_co_u32_e32 v85, vcc, 0, v83, vcc
	global_load_ushort v169, v[84:85], off
	global_load_ushort v170, v[84:85], off offset:2048
	v_add_co_u32_e32 v84, vcc, 0x4c022000, v82
	s_nop 1
	v_addc_co_u32_e32 v85, vcc, 0, v83, vcc
	v_add_co_u32_e32 v82, vcc, 0x4c023000, v82
	global_load_ushort v172, v[84:85], off
	global_load_ushort v173, v[84:85], off offset:2048
	v_addc_co_u32_e32 v83, vcc, 0, v83, vcc
	global_load_ushort v174, v[82:83], off
	global_load_ushort v175, v[82:83], off offset:2048
